# speedup vs baseline: 1.0465x; 1.0041x over previous
.Ltile0:
	s_mov_b32 s34, 0
	s_mul_i32 s35, s33, 0xa000
	v_add_u32_e32 v240, s35, v222
	v_add_u32_e32 v241, s35, v223
	v_add_u32_e32 v242, s35, v224
	s_add_u32 s33, s33, 1
	s_cmp_eq_u32 s33, 3
	s_cselect_b32 s33, 0, s33
	s_waitcnt vmcnt(5)
	s_waitcnt lgkmcnt(0)
	v_mfma_scale_f32_16x16x128_f8f6f4 v[0:3], v[128:131], v[160:165], 0, v208, v216 op_sel_hi:[0,0,0] cbsz:4 blgp:2
	v_mfma_scale_f32_16x16x128_f8f6f4 v[16:19], v[132:135], v[160:165], 0, v209, v216 op_sel_hi:[0,0,0] cbsz:4 blgp:2
	s_barrier
	ds_read_b128 v[244:247], v240 offset:6144
	ds_read_b128 v[252:255], v240 offset:7168
	v_mfma_scale_f32_16x16x128_f8f6f4 v[20:23], v[132:135], v[166:171], 0, v209, v217 op_sel_hi:[0,0,0] cbsz:4 blgp:2
	s_cmp_eq_u32 s34, 13
	s_cselect_b32 s36, s38, s36
	s_cselect_b32 s37, s39, s37
	s_mov_b32 m0, s40
	v_mfma_scale_f32_16x16x128_f8f6f4 v[4:7], v[128:131], v[166:171], 0, v208, v217 op_sel_hi:[0,0,0] cbsz:4 blgp:2
	ds_read_b128 v[184:187], v241 offset:0
	v_mfma_scale_f32_16x16x128_f8f6f4 v[8:11], v[128:131], v[172:177], 0, v208, v218 op_sel_hi:[0,0,0] cbsz:4 blgp:2
	buffer_load_dwordx4 v221, s[4:7], s36 offen lds
	v_mfma_scale_f32_16x16x128_f8f6f4 v[24:27], v[132:135], v[172:177], 0, v209, v218 op_sel_hi:[0,0,0] cbsz:4 blgp:2
	s_add_u32 m0, s40, 0x2000
	ds_read_b64 v[188:189], v242 offset:0
	v_mfma_scale_f32_16x16x128_f8f6f4 v[28:31], v[132:135], v[178:183], 0, v209, v219 op_sel_hi:[0,0,0] cbsz:4 blgp:2
	buffer_load_dwordx4 v225, s[4:7], s36 offen lds
	v_mfma_scale_f32_16x16x128_f8f6f4 v[12:15], v[128:131], v[178:183], 0, v208, v219 op_sel_hi:[0,0,0] cbsz:4 blgp:2
	s_add_u32 m0, s40, 0x4000
	ds_read_b128 v[190:193], v241 offset:1536
	v_mfma_scale_f32_16x16x128_f8f6f4 v[44:47], v[136:139], v[178:183], 0, v210, v219 op_sel_hi:[0,0,0] cbsz:4 blgp:2
	buffer_load_dwordx4 v221, s[4:7], s37 offen lds
	v_mfma_scale_f32_16x16x128_f8f6f4 v[60:63], v[140:143], v[178:183], 0, v211, v219 op_sel_hi:[0,0,0] cbsz:4 blgp:2
	s_add_u32 m0, s40, 0x6000
	ds_read_b64 v[194:195], v242 offset:1536
	v_mfma_scale_f32_16x16x128_f8f6f4 v[56:59], v[140:143], v[172:177], 0, v211, v218 op_sel_hi:[0,0,0] cbsz:4 blgp:2
	buffer_load_dwordx4 v225, s[4:7], s37 offen lds
	v_mfma_scale_f32_16x16x128_f8f6f4 v[40:43], v[136:139], v[172:177], 0, v210, v218 op_sel_hi:[0,0,0] cbsz:4 blgp:2
	s_add_u32 m0, s40, 0x8000
	ds_read_b128 v[196:199], v241 offset:3072
	v_mfma_scale_f32_16x16x128_f8f6f4 v[36:39], v[136:139], v[166:171], 0, v210, v217 op_sel_hi:[0,0,0] cbsz:4 blgp:2
	buffer_load_dwordx4 v226, s[4:7], s37 offen lds
	v_mfma_scale_f32_16x16x128_f8f6f4 v[52:55], v[140:143], v[166:171], 0, v211, v217 op_sel_hi:[0,0,0] cbsz:4 blgp:2
	ds_read_b64 v[200:201], v242 offset:3072
	v_mfma_scale_f32_16x16x128_f8f6f4 v[48:51], v[140:143], v[160:165], 0, v211, v216 op_sel_hi:[0,0,0] cbsz:4 blgp:2
	ds_read_b128 v[202:205], v241 offset:4608
	v_mfma_scale_f32_16x16x128_f8f6f4 v[32:35], v[136:139], v[160:165], 0, v210, v216 op_sel_hi:[0,0,0] cbsz:4 blgp:2
	ds_read_b64 v[206:207], v242 offset:4608
	v_mfma_scale_f32_16x16x128_f8f6f4 v[64:67], v[144:147], v[160:165], 0, v212, v216 op_sel_hi:[0,0,0] cbsz:4 blgp:2
	s_add_u32 s36, s36, 0x4000
	s_add_u32 s37, s37, 0x6000
	s_add_u32 s40, s40, 0xa000
	s_sub_u32 s41, s40, 0x1e000
	v_mfma_scale_f32_16x16x128_f8f6f4 v[80:83], v[148:151], v[160:165], 0, v213, v216 op_sel_hi:[0,0,0] cbsz:4 blgp:2
	s_cmp_ge_u32 s40, s49
	s_cselect_b32 s40, s41, s40
	ds_read_b128 v[132:135], v240 offset:1024
	v_mfma_scale_f32_16x16x128_f8f6f4 v[84:87], v[148:151], v[166:171], 0, v213, v217 op_sel_hi:[0,0,0] cbsz:4 blgp:2
	ds_read_b128 v[128:131], v240 offset:0
	v_mfma_scale_f32_16x16x128_f8f6f4 v[68:71], v[144:147], v[166:171], 0, v212, v217 op_sel_hi:[0,0,0] cbsz:4 blgp:2
	ds_read_b128 v[140:143], v240 offset:3072
	v_mfma_scale_f32_16x16x128_f8f6f4 v[72:75], v[144:147], v[172:177], 0, v212, v218 op_sel_hi:[0,0,0] cbsz:4 blgp:2
	ds_read_b128 v[136:139], v240 offset:2048
	v_mfma_scale_f32_16x16x128_f8f6f4 v[88:91], v[148:151], v[172:177], 0, v213, v218 op_sel_hi:[0,0,0] cbsz:4 blgp:2
	v_mfma_scale_f32_16x16x128_f8f6f4 v[92:95], v[148:151], v[178:183], 0, v213, v219 op_sel_hi:[0,0,0] cbsz:4 blgp:2
	v_mfma_scale_f32_16x16x128_f8f6f4 v[76:79], v[144:147], v[178:183], 0, v212, v219 op_sel_hi:[0,0,0] cbsz:4 blgp:2
	ds_read_b128 v[148:151], v240 offset:5120
	v_mfma_scale_f32_16x16x128_f8f6f4 v[108:111], v[152:155], v[178:183], 0, v214, v219 op_sel_hi:[0,0,0] cbsz:4 blgp:2
	ds_read_b128 v[144:147], v240 offset:4096
	v_mfma_scale_f32_16x16x128_f8f6f4 v[124:127], v[156:159], v[178:183], 0, v215, v219 op_sel_hi:[0,0,0] cbsz:4 blgp:2
	v_mfma_scale_f32_16x16x128_f8f6f4 v[120:123], v[156:159], v[172:177], 0, v215, v218 op_sel_hi:[0,0,0] cbsz:4 blgp:2
	v_mfma_scale_f32_16x16x128_f8f6f4 v[104:107], v[152:155], v[172:177], 0, v214, v218 op_sel_hi:[0,0,0] cbsz:4 blgp:2
	v_mfma_scale_f32_16x16x128_f8f6f4 v[100:103], v[152:155], v[166:171], 0, v214, v217 op_sel_hi:[0,0,0] cbsz:4 blgp:2
	v_mfma_scale_f32_16x16x128_f8f6f4 v[116:119], v[156:159], v[166:171], 0, v215, v217 op_sel_hi:[0,0,0] cbsz:4 blgp:2
	v_mfma_scale_f32_16x16x128_f8f6f4 v[112:115], v[156:159], v[160:165], 0, v215, v216 op_sel_hi:[0,0,0] cbsz:4 blgp:2
	v_mfma_scale_f32_16x16x128_f8f6f4 v[96:99], v[152:155], v[160:165], 0, v214, v216 op_sel_hi:[0,0,0] cbsz:4 blgp:2
	s_add_u32 s34, s34, 1
	s_mul_i32 s35, s33, 0xa000
	v_add_u32_e32 v240, s35, v222
	v_add_u32_e32 v241, s35, v223
	v_add_u32_e32 v242, s35, v224
	s_add_u32 s33, s33, 1
	s_cmp_eq_u32 s33, 3
	s_cselect_b32 s33, 0, s33
	s_waitcnt vmcnt(5)
	s_waitcnt lgkmcnt(0)
	v_mfma_scale_f32_16x16x128_f8f6f4 v[0:3], v[128:131], v[184:189], v[0:3], v208, v216 op_sel_hi:[0,0,0] cbsz:4 blgp:2
	v_mfma_scale_f32_16x16x128_f8f6f4 v[16:19], v[132:135], v[184:189], v[16:19], v209, v216 op_sel_hi:[0,0,0] cbsz:4 blgp:2
	s_barrier
	ds_read_b128 v[152:155], v240 offset:6144
	ds_read_b128 v[156:159], v240 offset:7168
	v_mfma_scale_f32_16x16x128_f8f6f4 v[20:23], v[132:135], v[190:195], v[20:23], v209, v217 op_sel_hi:[0,0,0] cbsz:4 blgp:2
	s_cmp_eq_u32 s34, 13
	s_cselect_b32 s36, s38, s36
	s_cselect_b32 s37, s39, s37
	s_mov_b32 m0, s40
	v_mfma_scale_f32_16x16x128_f8f6f4 v[4:7], v[128:131], v[190:195], v[4:7], v208, v217 op_sel_hi:[0,0,0] cbsz:4 blgp:2
	ds_read_b128 v[160:163], v241 offset:0
	v_mfma_scale_f32_16x16x128_f8f6f4 v[8:11], v[128:131], v[196:201], v[8:11], v208, v218 op_sel_hi:[0,0,0] cbsz:4 blgp:2
	buffer_load_dwordx4 v221, s[4:7], s36 offen lds
	v_mfma_scale_f32_16x16x128_f8f6f4 v[24:27], v[132:135], v[196:201], v[24:27], v209, v218 op_sel_hi:[0,0,0] cbsz:4 blgp:2
	s_add_u32 m0, s40, 0x2000
	ds_read_b64 v[164:165], v242 offset:0
	v_mfma_scale_f32_16x16x128_f8f6f4 v[28:31], v[132:135], v[202:207], v[28:31], v209, v219 op_sel_hi:[0,0,0] cbsz:4 blgp:2
	buffer_load_dwordx4 v225, s[4:7], s36 offen lds
	v_mfma_scale_f32_16x16x128_f8f6f4 v[12:15], v[128:131], v[202:207], v[12:15], v208, v219 op_sel_hi:[0,0,0] cbsz:4 blgp:2
	s_add_u32 m0, s40, 0x4000
	ds_read_b128 v[166:169], v241 offset:1536
	v_mfma_scale_f32_16x16x128_f8f6f4 v[44:47], v[136:139], v[202:207], v[44:47], v210, v219 op_sel_hi:[0,0,0] cbsz:4 blgp:2
	buffer_load_dwordx4 v221, s[4:7], s37 offen lds
	v_mfma_scale_f32_16x16x128_f8f6f4 v[60:63], v[140:143], v[202:207], v[60:63], v211, v219 op_sel_hi:[0,0,0] cbsz:4 blgp:2
	s_add_u32 m0, s40, 0x6000
	ds_read_b64 v[170:171], v242 offset:1536
	v_mfma_scale_f32_16x16x128_f8f6f4 v[56:59], v[140:143], v[196:201], v[56:59], v211, v218 op_sel_hi:[0,0,0] cbsz:4 blgp:2
	buffer_load_dwordx4 v225, s[4:7], s37 offen lds
	v_mfma_scale_f32_16x16x128_f8f6f4 v[40:43], v[136:139], v[196:201], v[40:43], v210, v218 op_sel_hi:[0,0,0] cbsz:4 blgp:2
	s_add_u32 m0, s40, 0x8000
	ds_read_b128 v[172:175], v241 offset:3072
	v_mfma_scale_f32_16x16x128_f8f6f4 v[36:39], v[136:139], v[190:195], v[36:39], v210, v217 op_sel_hi:[0,0,0] cbsz:4 blgp:2
	buffer_load_dwordx4 v226, s[4:7], s37 offen lds
	v_mfma_scale_f32_16x16x128_f8f6f4 v[52:55], v[140:143], v[190:195], v[52:55], v211, v217 op_sel_hi:[0,0,0] cbsz:4 blgp:2
	ds_read_b64 v[176:177], v242 offset:3072
	v_mfma_scale_f32_16x16x128_f8f6f4 v[48:51], v[140:143], v[184:189], v[48:51], v211, v216 op_sel_hi:[0,0,0] cbsz:4 blgp:2
	ds_read_b128 v[178:181], v241 offset:4608
	v_mfma_scale_f32_16x16x128_f8f6f4 v[32:35], v[136:139], v[184:189], v[32:35], v210, v216 op_sel_hi:[0,0,0] cbsz:4 blgp:2
	ds_read_b64 v[182:183], v242 offset:4608
	v_mfma_scale_f32_16x16x128_f8f6f4 v[64:67], v[144:147], v[184:189], v[64:67], v212, v216 op_sel_hi:[0,0,0] cbsz:4 blgp:2
	s_add_u32 s36, s36, 0x4000
	s_add_u32 s37, s37, 0x6000
	s_add_u32 s40, s40, 0xa000
	s_sub_u32 s41, s40, 0x1e000
	v_mfma_scale_f32_16x16x128_f8f6f4 v[80:83], v[148:151], v[184:189], v[80:83], v213, v216 op_sel_hi:[0,0,0] cbsz:4 blgp:2
	s_cmp_ge_u32 s40, s49
	s_cselect_b32 s40, s41, s40
	ds_read_b128 v[132:135], v240 offset:1024
	v_mfma_scale_f32_16x16x128_f8f6f4 v[84:87], v[148:151], v[190:195], v[84:87], v213, v217 op_sel_hi:[0,0,0] cbsz:4 blgp:2
	ds_read_b128 v[128:131], v240 offset:0
	v_mfma_scale_f32_16x16x128_f8f6f4 v[68:71], v[144:147], v[190:195], v[68:71], v212, v217 op_sel_hi:[0,0,0] cbsz:4 blgp:2
	ds_read_b128 v[140:143], v240 offset:3072
	v_mfma_scale_f32_16x16x128_f8f6f4 v[72:75], v[144:147], v[196:201], v[72:75], v212, v218 op_sel_hi:[0,0,0] cbsz:4 blgp:2
	ds_read_b128 v[136:139], v240 offset:2048
	v_mfma_scale_f32_16x16x128_f8f6f4 v[88:91], v[148:151], v[196:201], v[88:91], v213, v218 op_sel_hi:[0,0,0] cbsz:4 blgp:2
	v_mfma_scale_f32_16x16x128_f8f6f4 v[92:95], v[148:151], v[202:207], v[92:95], v213, v219 op_sel_hi:[0,0,0] cbsz:4 blgp:2
	v_mfma_scale_f32_16x16x128_f8f6f4 v[76:79], v[144:147], v[202:207], v[76:79], v212, v219 op_sel_hi:[0,0,0] cbsz:4 blgp:2
	ds_read_b128 v[148:151], v240 offset:5120
	v_mfma_scale_f32_16x16x128_f8f6f4 v[108:111], v[244:247], v[202:207], v[108:111], v214, v219 op_sel_hi:[0,0,0] cbsz:4 blgp:2
	ds_read_b128 v[144:147], v240 offset:4096
	v_mfma_scale_f32_16x16x128_f8f6f4 v[124:127], v[252:255], v[202:207], v[124:127], v215, v219 op_sel_hi:[0,0,0] cbsz:4 blgp:2
	v_mfma_scale_f32_16x16x128_f8f6f4 v[120:123], v[252:255], v[196:201], v[120:123], v215, v218 op_sel_hi:[0,0,0] cbsz:4 blgp:2
	v_mfma_scale_f32_16x16x128_f8f6f4 v[104:107], v[244:247], v[196:201], v[104:107], v214, v218 op_sel_hi:[0,0,0] cbsz:4 blgp:2
	v_mfma_scale_f32_16x16x128_f8f6f4 v[100:103], v[244:247], v[190:195], v[100:103], v214, v217 op_sel_hi:[0,0,0] cbsz:4 blgp:2
	v_mfma_scale_f32_16x16x128_f8f6f4 v[116:119], v[252:255], v[190:195], v[116:119], v215, v217 op_sel_hi:[0,0,0] cbsz:4 blgp:2
	v_mfma_scale_f32_16x16x128_f8f6f4 v[112:115], v[252:255], v[184:189], v[112:115], v215, v216 op_sel_hi:[0,0,0] cbsz:4 blgp:2
	v_mfma_scale_f32_16x16x128_f8f6f4 v[96:99], v[244:247], v[184:189], v[96:99], v214, v216 op_sel_hi:[0,0,0] cbsz:4 blgp:2
	s_add_u32 s34, s34, 1
.Lkloop0:
	s_mul_i32 s35, s33, 0xa000
	v_add_u32_e32 v240, s35, v222
	v_add_u32_e32 v241, s35, v223
	v_add_u32_e32 v242, s35, v224
	s_add_u32 s33, s33, 1
	s_cmp_eq_u32 s33, 3
	s_cselect_b32 s33, 0, s33
	s_waitcnt vmcnt(5)
	s_waitcnt lgkmcnt(0)
	v_mfma_scale_f32_16x16x128_f8f6f4 v[0:3], v[128:131], v[160:165], v[0:3], v208, v216 op_sel_hi:[0,0,0] cbsz:4 blgp:2
	v_mfma_scale_f32_16x16x128_f8f6f4 v[16:19], v[132:135], v[160:165], v[16:19], v209, v216 op_sel_hi:[0,0,0] cbsz:4 blgp:2
	s_barrier
	ds_read_b128 v[244:247], v240 offset:6144
	ds_read_b128 v[252:255], v240 offset:7168
	v_mfma_scale_f32_16x16x128_f8f6f4 v[20:23], v[132:135], v[166:171], v[20:23], v209, v217 op_sel_hi:[0,0,0] cbsz:4 blgp:2
	s_cmp_eq_u32 s34, 13
	s_cselect_b32 s36, s38, s36
	s_cselect_b32 s37, s39, s37
	s_mov_b32 m0, s40
	v_mfma_scale_f32_16x16x128_f8f6f4 v[4:7], v[128:131], v[166:171], v[4:7], v208, v217 op_sel_hi:[0,0,0] cbsz:4 blgp:2
	ds_read_b128 v[184:187], v241 offset:0
	v_mfma_scale_f32_16x16x128_f8f6f4 v[8:11], v[128:131], v[172:177], v[8:11], v208, v218 op_sel_hi:[0,0,0] cbsz:4 blgp:2
	buffer_load_dwordx4 v221, s[4:7], s36 offen lds
	v_mfma_scale_f32_16x16x128_f8f6f4 v[24:27], v[132:135], v[172:177], v[24:27], v209, v218 op_sel_hi:[0,0,0] cbsz:4 blgp:2
	s_add_u32 m0, s40, 0x2000
	ds_read_b64 v[188:189], v242 offset:0
	v_mfma_scale_f32_16x16x128_f8f6f4 v[28:31], v[132:135], v[178:183], v[28:31], v209, v219 op_sel_hi:[0,0,0] cbsz:4 blgp:2
	buffer_load_dwordx4 v225, s[4:7], s36 offen lds
	v_mfma_scale_f32_16x16x128_f8f6f4 v[12:15], v[128:131], v[178:183], v[12:15], v208, v219 op_sel_hi:[0,0,0] cbsz:4 blgp:2
	s_add_u32 m0, s40, 0x4000
	ds_read_b128 v[190:193], v241 offset:1536
	v_mfma_scale_f32_16x16x128_f8f6f4 v[44:47], v[136:139], v[178:183], v[44:47], v210, v219 op_sel_hi:[0,0,0] cbsz:4 blgp:2
	buffer_load_dwordx4 v221, s[4:7], s37 offen lds
	v_mfma_scale_f32_16x16x128_f8f6f4 v[60:63], v[140:143], v[178:183], v[60:63], v211, v219 op_sel_hi:[0,0,0] cbsz:4 blgp:2
	s_add_u32 m0, s40, 0x6000
	ds_read_b64 v[194:195], v242 offset:1536
	v_mfma_scale_f32_16x16x128_f8f6f4 v[56:59], v[140:143], v[172:177], v[56:59], v211, v218 op_sel_hi:[0,0,0] cbsz:4 blgp:2
	buffer_load_dwordx4 v225, s[4:7], s37 offen lds
	v_mfma_scale_f32_16x16x128_f8f6f4 v[40:43], v[136:139], v[172:177], v[40:43], v210, v218 op_sel_hi:[0,0,0] cbsz:4 blgp:2
	s_add_u32 m0, s40, 0x8000
	ds_read_b128 v[196:199], v241 offset:3072
	v_mfma_scale_f32_16x16x128_f8f6f4 v[36:39], v[136:139], v[166:171], v[36:39], v210, v217 op_sel_hi:[0,0,0] cbsz:4 blgp:2
	buffer_load_dwordx4 v226, s[4:7], s37 offen lds
	v_mfma_scale_f32_16x16x128_f8f6f4 v[52:55], v[140:143], v[166:171], v[52:55], v211, v217 op_sel_hi:[0,0,0] cbsz:4 blgp:2
	ds_read_b64 v[200:201], v242 offset:3072
	v_mfma_scale_f32_16x16x128_f8f6f4 v[48:51], v[140:143], v[160:165], v[48:51], v211, v216 op_sel_hi:[0,0,0] cbsz:4 blgp:2
	ds_read_b128 v[202:205], v241 offset:4608
	v_mfma_scale_f32_16x16x128_f8f6f4 v[32:35], v[136:139], v[160:165], v[32:35], v210, v216 op_sel_hi:[0,0,0] cbsz:4 blgp:2
	ds_read_b64 v[206:207], v242 offset:4608
	v_mfma_scale_f32_16x16x128_f8f6f4 v[64:67], v[144:147], v[160:165], v[64:67], v212, v216 op_sel_hi:[0,0,0] cbsz:4 blgp:2
	s_add_u32 s36, s36, 0x4000
	s_add_u32 s37, s37, 0x6000
	s_add_u32 s40, s40, 0xa000
	s_sub_u32 s41, s40, 0x1e000
	v_mfma_scale_f32_16x16x128_f8f6f4 v[80:83], v[148:151], v[160:165], v[80:83], v213, v216 op_sel_hi:[0,0,0] cbsz:4 blgp:2
	s_cmp_ge_u32 s40, s49
	s_cselect_b32 s40, s41, s40
	ds_read_b128 v[132:135], v240 offset:1024
	v_mfma_scale_f32_16x16x128_f8f6f4 v[84:87], v[148:151], v[166:171], v[84:87], v213, v217 op_sel_hi:[0,0,0] cbsz:4 blgp:2
	ds_read_b128 v[128:131], v240 offset:0
	v_mfma_scale_f32_16x16x128_f8f6f4 v[68:71], v[144:147], v[166:171], v[68:71], v212, v217 op_sel_hi:[0,0,0] cbsz:4 blgp:2
	ds_read_b128 v[140:143], v240 offset:3072
	v_mfma_scale_f32_16x16x128_f8f6f4 v[72:75], v[144:147], v[172:177], v[72:75], v212, v218 op_sel_hi:[0,0,0] cbsz:4 blgp:2
	ds_read_b128 v[136:139], v240 offset:2048
	v_mfma_scale_f32_16x16x128_f8f6f4 v[88:91], v[148:151], v[172:177], v[88:91], v213, v218 op_sel_hi:[0,0,0] cbsz:4 blgp:2
	v_mfma_scale_f32_16x16x128_f8f6f4 v[92:95], v[148:151], v[178:183], v[92:95], v213, v219 op_sel_hi:[0,0,0] cbsz:4 blgp:2
	v_mfma_scale_f32_16x16x128_f8f6f4 v[76:79], v[144:147], v[178:183], v[76:79], v212, v219 op_sel_hi:[0,0,0] cbsz:4 blgp:2
	ds_read_b128 v[148:151], v240 offset:5120
	v_mfma_scale_f32_16x16x128_f8f6f4 v[108:111], v[152:155], v[178:183], v[108:111], v214, v219 op_sel_hi:[0,0,0] cbsz:4 blgp:2
	ds_read_b128 v[144:147], v240 offset:4096
	v_mfma_scale_f32_16x16x128_f8f6f4 v[124:127], v[156:159], v[178:183], v[124:127], v215, v219 op_sel_hi:[0,0,0] cbsz:4 blgp:2
	v_mfma_scale_f32_16x16x128_f8f6f4 v[120:123], v[156:159], v[172:177], v[120:123], v215, v218 op_sel_hi:[0,0,0] cbsz:4 blgp:2
	v_mfma_scale_f32_16x16x128_f8f6f4 v[104:107], v[152:155], v[172:177], v[104:107], v214, v218 op_sel_hi:[0,0,0] cbsz:4 blgp:2
	v_mfma_scale_f32_16x16x128_f8f6f4 v[100:103], v[152:155], v[166:171], v[100:103], v214, v217 op_sel_hi:[0,0,0] cbsz:4 blgp:2
	v_mfma_scale_f32_16x16x128_f8f6f4 v[116:119], v[156:159], v[166:171], v[116:119], v215, v217 op_sel_hi:[0,0,0] cbsz:4 blgp:2
	v_mfma_scale_f32_16x16x128_f8f6f4 v[112:115], v[156:159], v[160:165], v[112:115], v215, v216 op_sel_hi:[0,0,0] cbsz:4 blgp:2
	v_mfma_scale_f32_16x16x128_f8f6f4 v[96:99], v[152:155], v[160:165], v[96:99], v214, v216 op_sel_hi:[0,0,0] cbsz:4 blgp:2
	s_add_u32 s34, s34, 1
	s_mul_i32 s35, s33, 0xa000
	v_add_u32_e32 v240, s35, v222
	v_add_u32_e32 v241, s35, v223
	v_add_u32_e32 v242, s35, v224
	s_add_u32 s33, s33, 1
	s_cmp_eq_u32 s33, 3
	s_cselect_b32 s33, 0, s33
	s_waitcnt vmcnt(5)
	s_waitcnt lgkmcnt(0)
	v_mfma_scale_f32_16x16x128_f8f6f4 v[0:3], v[128:131], v[184:189], v[0:3], v208, v216 op_sel_hi:[0,0,0] cbsz:4 blgp:2
	v_mfma_scale_f32_16x16x128_f8f6f4 v[16:19], v[132:135], v[184:189], v[16:19], v209, v216 op_sel_hi:[0,0,0] cbsz:4 blgp:2
	s_barrier
	ds_read_b128 v[152:155], v240 offset:6144
	ds_read_b128 v[156:159], v240 offset:7168
	v_mfma_scale_f32_16x16x128_f8f6f4 v[20:23], v[132:135], v[190:195], v[20:23], v209, v217 op_sel_hi:[0,0,0] cbsz:4 blgp:2
	s_cmp_eq_u32 s34, 13
	s_cselect_b32 s36, s38, s36
	s_cselect_b32 s37, s39, s37
	s_mov_b32 m0, s40
	v_mfma_scale_f32_16x16x128_f8f6f4 v[4:7], v[128:131], v[190:195], v[4:7], v208, v217 op_sel_hi:[0,0,0] cbsz:4 blgp:2
	ds_read_b128 v[160:163], v241 offset:0
	v_mfma_scale_f32_16x16x128_f8f6f4 v[8:11], v[128:131], v[196:201], v[8:11], v208, v218 op_sel_hi:[0,0,0] cbsz:4 blgp:2
	buffer_load_dwordx4 v221, s[4:7], s36 offen lds
	v_mfma_scale_f32_16x16x128_f8f6f4 v[24:27], v[132:135], v[196:201], v[24:27], v209, v218 op_sel_hi:[0,0,0] cbsz:4 blgp:2
	s_add_u32 m0, s40, 0x2000
	ds_read_b64 v[164:165], v242 offset:0
	v_mfma_scale_f32_16x16x128_f8f6f4 v[28:31], v[132:135], v[202:207], v[28:31], v209, v219 op_sel_hi:[0,0,0] cbsz:4 blgp:2
	buffer_load_dwordx4 v225, s[4:7], s36 offen lds
	v_mfma_scale_f32_16x16x128_f8f6f4 v[12:15], v[128:131], v[202:207], v[12:15], v208, v219 op_sel_hi:[0,0,0] cbsz:4 blgp:2
	s_add_u32 m0, s40, 0x4000
	ds_read_b128 v[166:169], v241 offset:1536
	v_mfma_scale_f32_16x16x128_f8f6f4 v[44:47], v[136:139], v[202:207], v[44:47], v210, v219 op_sel_hi:[0,0,0] cbsz:4 blgp:2
	buffer_load_dwordx4 v221, s[4:7], s37 offen lds
	v_mfma_scale_f32_16x16x128_f8f6f4 v[60:63], v[140:143], v[202:207], v[60:63], v211, v219 op_sel_hi:[0,0,0] cbsz:4 blgp:2
	s_add_u32 m0, s40, 0x6000
	ds_read_b64 v[170:171], v242 offset:1536
	v_mfma_scale_f32_16x16x128_f8f6f4 v[56:59], v[140:143], v[196:201], v[56:59], v211, v218 op_sel_hi:[0,0,0] cbsz:4 blgp:2
	buffer_load_dwordx4 v225, s[4:7], s37 offen lds
	v_mfma_scale_f32_16x16x128_f8f6f4 v[40:43], v[136:139], v[196:201], v[40:43], v210, v218 op_sel_hi:[0,0,0] cbsz:4 blgp:2
	s_add_u32 m0, s40, 0x8000
	ds_read_b128 v[172:175], v241 offset:3072
	v_mfma_scale_f32_16x16x128_f8f6f4 v[36:39], v[136:139], v[190:195], v[36:39], v210, v217 op_sel_hi:[0,0,0] cbsz:4 blgp:2
	buffer_load_dwordx4 v226, s[4:7], s37 offen lds
	v_mfma_scale_f32_16x16x128_f8f6f4 v[52:55], v[140:143], v[190:195], v[52:55], v211, v217 op_sel_hi:[0,0,0] cbsz:4 blgp:2
	ds_read_b64 v[176:177], v242 offset:3072
	v_mfma_scale_f32_16x16x128_f8f6f4 v[48:51], v[140:143], v[184:189], v[48:51], v211, v216 op_sel_hi:[0,0,0] cbsz:4 blgp:2
	ds_read_b128 v[178:181], v241 offset:4608
	v_mfma_scale_f32_16x16x128_f8f6f4 v[32:35], v[136:139], v[184:189], v[32:35], v210, v216 op_sel_hi:[0,0,0] cbsz:4 blgp:2
	ds_read_b64 v[182:183], v242 offset:4608
	v_mfma_scale_f32_16x16x128_f8f6f4 v[64:67], v[144:147], v[184:189], v[64:67], v212, v216 op_sel_hi:[0,0,0] cbsz:4 blgp:2
	s_add_u32 s36, s36, 0x4000
	s_add_u32 s37, s37, 0x6000
	s_add_u32 s40, s40, 0xa000
	s_sub_u32 s41, s40, 0x1e000
	v_mfma_scale_f32_16x16x128_f8f6f4 v[80:83], v[148:151], v[184:189], v[80:83], v213, v216 op_sel_hi:[0,0,0] cbsz:4 blgp:2
	s_cmp_ge_u32 s40, s49
	s_cselect_b32 s40, s41, s40
	ds_read_b128 v[132:135], v240 offset:1024
	v_mfma_scale_f32_16x16x128_f8f6f4 v[84:87], v[148:151], v[190:195], v[84:87], v213, v217 op_sel_hi:[0,0,0] cbsz:4 blgp:2
	ds_read_b128 v[128:131], v240 offset:0
	v_mfma_scale_f32_16x16x128_f8f6f4 v[68:71], v[144:147], v[190:195], v[68:71], v212, v217 op_sel_hi:[0,0,0] cbsz:4 blgp:2
	ds_read_b128 v[140:143], v240 offset:3072
	v_mfma_scale_f32_16x16x128_f8f6f4 v[72:75], v[144:147], v[196:201], v[72:75], v212, v218 op_sel_hi:[0,0,0] cbsz:4 blgp:2
	ds_read_b128 v[136:139], v240 offset:2048
	v_mfma_scale_f32_16x16x128_f8f6f4 v[88:91], v[148:151], v[196:201], v[88:91], v213, v218 op_sel_hi:[0,0,0] cbsz:4 blgp:2
	v_mfma_scale_f32_16x16x128_f8f6f4 v[92:95], v[148:151], v[202:207], v[92:95], v213, v219 op_sel_hi:[0,0,0] cbsz:4 blgp:2
	v_mfma_scale_f32_16x16x128_f8f6f4 v[76:79], v[144:147], v[202:207], v[76:79], v212, v219 op_sel_hi:[0,0,0] cbsz:4 blgp:2
	ds_read_b128 v[148:151], v240 offset:5120
	v_mfma_scale_f32_16x16x128_f8f6f4 v[108:111], v[244:247], v[202:207], v[108:111], v214, v219 op_sel_hi:[0,0,0] cbsz:4 blgp:2
	ds_read_b128 v[144:147], v240 offset:4096
	v_mfma_scale_f32_16x16x128_f8f6f4 v[124:127], v[252:255], v[202:207], v[124:127], v215, v219 op_sel_hi:[0,0,0] cbsz:4 blgp:2
	v_mfma_scale_f32_16x16x128_f8f6f4 v[120:123], v[252:255], v[196:201], v[120:123], v215, v218 op_sel_hi:[0,0,0] cbsz:4 blgp:2
	v_mfma_scale_f32_16x16x128_f8f6f4 v[104:107], v[244:247], v[196:201], v[104:107], v214, v218 op_sel_hi:[0,0,0] cbsz:4 blgp:2
	v_mfma_scale_f32_16x16x128_f8f6f4 v[100:103], v[244:247], v[190:195], v[100:103], v214, v217 op_sel_hi:[0,0,0] cbsz:4 blgp:2
	v_mfma_scale_f32_16x16x128_f8f6f4 v[116:119], v[252:255], v[190:195], v[116:119], v215, v217 op_sel_hi:[0,0,0] cbsz:4 blgp:2
	v_mfma_scale_f32_16x16x128_f8f6f4 v[112:115], v[252:255], v[184:189], v[112:115], v215, v216 op_sel_hi:[0,0,0] cbsz:4 blgp:2
	v_mfma_scale_f32_16x16x128_f8f6f4 v[96:99], v[244:247], v[184:189], v[96:99], v214, v216 op_sel_hi:[0,0,0] cbsz:4 blgp:2
	s_cmp_eq_u32 s34, 13
	s_cbranch_scc0 .Lnosc_or0
	s_add_u32 s44, s23, 1
	s_and_b32 s44, s44, 1
	s_cmp_lt_u32 s18, 4
	s_cselect_b32 s80, s26, s27
	s_cselect_b32 s82, s8, s10
	s_cselect_b32 s83, s9, s11
	s_lshl_b32 s80, s80, 10
	s_and_b32 s84, s18, 3
	s_lshl_b32 s84, s84, 8
	s_add_u32 s80, s80, s84
	s_add_u32 s82, s82, s80
	s_addc_u32 s83, s83, 0
	s_lshl_b32 s84, s44, 11
	s_lshl_b32 s85, s18, 8
	s_add_u32 s84, s84, s85
	s_add_u32 s84, s84, 0x1e000
	s_mov_b32 m0, s84
	v_lshlrev_b32_e32 v236, 2, v220
	global_load_lds_dword v236, s[82:83]
